# v47 + grid barrier release flattened: non-last workgroups spin on the top generation word instead of the per-XCD one; per-XCD release atomic dropped
# baseline (speedup 1.0000x reference)
; DI unsigned xb_ld(unsigned* p)              { return __hip_atomic_load(p, __ATOMIC_RELAXED, __HIP_MEMORY_SCOPE_AGENT); }
; DI unsigned xb_add(unsigned* p, unsigned v) { return __hip_atomic_fetch_add(p, v, __ATOMIC_RELAXED, __HIP_MEMORY_SCOPE_AGENT); }
; #define XB_SPIN(cond, bar) do { unsigned _sp = 0; while (cond) { __builtin_amdgcn_s_sleep(1); \
;     if ((++_sp & 255u) == 0u) { if (xb_ld(&(bar)[XB_TMO])) break; if (_sp > XB_SPIN_CAP) { atomicAdd(&(bar)[XB_TMO], 1u); break; } } } } while (0)
; DI void xcd_barrier(const XcdBarrier& b) {
;     ...
;         const unsigned old = xb_add(&bar[XB_XSUB(b.x)], 1u);
;         const unsigned gen = old / nloc;
;         if (old + 1u == (gen + 1u) * nloc) {
;             __builtin_amdgcn_fence(__ATOMIC_RELEASE, "agent");
;             asm volatile("s_waitcnt vmcnt(0)" ::: "memory");
;             const unsigned og = xb_add(&bar[XB_TOP], 1u);
;             const unsigned tg = og / nx;
;             if (og + 1u == (tg + 1u) * nx) xb_add(&bar[XB_TOPGEN], 1u);
;             else XB_SPIN(xb_ld(&bar[XB_TOPGEN]) == tg, bar);
;             __builtin_amdgcn_fence(__ATOMIC_ACQUIRE, "agent");
;             xb_add(&bar[XB_XGEN(b.x)], 1u);
;             asm volatile("s_waitcnt vmcnt(0)" ::: "memory");
;         } else {
;             XB_SPIN(xb_ld(&bar[XB_XGEN(b.x)]) == gen, bar);
.LBB0_32:
	s_or_b64 exec, exec, s[12:13]
	v_cvt_f32_u32_e32 v4, v2
	s_waitcnt vmcnt(0)
	v_readfirstlane_b32 s3, v3
	v_sub_u32_e32 v3, 0, v2
	v_rcp_iflag_f32_e32 v4, v4
	v_add_u32_e32 v5, s3, v1
	v_mul_f32_e32 v4, 0x4f7ffffe, v4
	v_cvt_u32_f32_e32 v4, v4
	v_mul_lo_u32 v1, v3, v4
	v_mul_hi_u32 v1, v4, v1
	v_add_u32_e32 v1, v4, v1
	v_mul_hi_u32 v1, v5, v1
	v_mul_lo_u32 v3, v1, v2
	v_sub_u32_e32 v3, v5, v3
	v_add_u32_e32 v4, 1, v1
	v_cmp_ge_u32_e32 vcc, v3, v2
	s_nop 1
	v_cndmask_b32_e32 v1, v1, v4, vcc
	v_sub_u32_e32 v4, v3, v2
	v_cndmask_b32_e32 v3, v3, v4, vcc
	v_add_u32_e32 v4, 1, v1
	v_cmp_ge_u32_e32 vcc, v3, v2
	v_add_u32_e32 v3, 1, v5
	s_nop 0
	v_cndmask_b32_e32 v1, v1, v4, vcc
	v_mul_lo_u32 v4, v2, v1
	v_add_u32_e32 v2, v4, v2
	v_cmp_ne_u32_e32 vcc, v3, v2
	s_and_saveexec_b64 s[4:5], vcc
	s_xor_b64 s[10:11], exec, s[4:5]
	s_cbranch_execz .LBB0_46
	s_waitcnt lgkmcnt(0)
	v_mov_b32_e32 v0, 0x3500
	global_load_dword v0, v0, s[34:35] sc1
	s_add_u32 s14, s34, 0x3500
	s_addc_u32 s15, s35, 0
	s_waitcnt vmcnt(0)
	v_cmp_eq_u32_e32 vcc, v0, v1
	s_and_saveexec_b64 s[12:13], vcc
	s_cbranch_execz .LBB0_45
	s_mov_b32 s3, 1
	s_mov_b64 s[16:17], 0
	v_mov_b32_e32 v0, 0
	s_branch .LBB0_36

; DI unsigned xb_add(unsigned* p, unsigned v) { return __hip_atomic_fetch_add(p, v, __ATOMIC_RELAXED, __HIP_MEMORY_SCOPE_AGENT); }
; DI void xcd_barrier(const XcdBarrier& b) {
;     ...
;             __builtin_amdgcn_fence(__ATOMIC_ACQUIRE, "agent");
;             xb_add(&bar[XB_XGEN(b.x)], 1u);
;             asm volatile("s_waitcnt vmcnt(0)" ::: "memory");
.LBB0_63:
	s_or_b64 exec, exec, s[10:11]
	s_mov_b64 s[10:11], exec
	v_mbcnt_lo_u32_b32 v0, s10, 0
	v_mbcnt_hi_u32_b32 v0, s11, v0
	v_cmp_eq_u32_e32 vcc, 0, v0
	s_waitcnt vmcnt(0)
	buffer_inv sc1
	s_and_saveexec_b64 s[12:13], vcc
	s_cbranch_execz .LBB0_65
	s_bcnt1_i32_b64 s3, s[10:11]
	v_mov_b32_e32 v0, 0x2000
	v_mov_b32_e32 v1, s3
.LBB0_65:
	s_or_b64 exec, exec, s[12:13]
	s_waitcnt vmcnt(0)

; DI unsigned xb_add(unsigned* p, unsigned v) { return __hip_atomic_fetch_add(p, v, __ATOMIC_RELAXED, __HIP_MEMORY_SCOPE_AGENT); }
; DI void xcd_barrier(const XcdBarrier& b) {
;     ...
;             __builtin_amdgcn_fence(__ATOMIC_ACQUIRE, "agent");
;             xb_add(&bar[XB_XGEN(b.x)], 1u);
;             asm volatile("s_waitcnt vmcnt(0)" ::: "memory");
.LBB0_125:
	s_or_b64 exec, exec, s[10:11]
	s_mov_b64 s[10:11], exec
	v_mbcnt_lo_u32_b32 v0, s10, 0
	v_mbcnt_hi_u32_b32 v0, s11, v0
	v_cmp_eq_u32_e32 vcc, 0, v0
	s_waitcnt vmcnt(0)
	buffer_inv sc1
	s_and_saveexec_b64 s[12:13], vcc
	s_cbranch_execz .LBB0_127
	s_bcnt1_i32_b64 s3, s[10:11]
	v_mov_b32_e32 v0, 0x2000
	v_mov_b32_e32 v1, s3
.LBB0_127:
	s_or_b64 exec, exec, s[12:13]
	s_waitcnt vmcnt(0)

; DI unsigned xb_ld(unsigned* p)              { return __hip_atomic_load(p, __ATOMIC_RELAXED, __HIP_MEMORY_SCOPE_AGENT); }
; DI unsigned xb_add(unsigned* p, unsigned v) { return __hip_atomic_fetch_add(p, v, __ATOMIC_RELAXED, __HIP_MEMORY_SCOPE_AGENT); }
; #define XB_SPIN(cond, bar) do { unsigned _sp = 0; while (cond) { __builtin_amdgcn_s_sleep(1); \
;     if ((++_sp & 255u) == 0u) { if (xb_ld(&(bar)[XB_TMO])) break; if (_sp > XB_SPIN_CAP) { atomicAdd(&(bar)[XB_TMO], 1u); break; } } } } while (0)
; DI void xcd_barrier(const XcdBarrier& b) {
;     ...
;         const unsigned old = xb_add(&bar[XB_XSUB(b.x)], 1u);
;         const unsigned gen = old / nloc;
;         if (old + 1u == (gen + 1u) * nloc) {
;             __builtin_amdgcn_fence(__ATOMIC_RELEASE, "agent");
;             asm volatile("s_waitcnt vmcnt(0)" ::: "memory");
;             const unsigned og = xb_add(&bar[XB_TOP], 1u);
;             const unsigned tg = og / nx;
;             if (og + 1u == (tg + 1u) * nx) xb_add(&bar[XB_TOPGEN], 1u);
;             else XB_SPIN(xb_ld(&bar[XB_TOPGEN]) == tg, bar);
;             __builtin_amdgcn_fence(__ATOMIC_ACQUIRE, "agent");
;             xb_add(&bar[XB_XGEN(b.x)], 1u);
;             asm volatile("s_waitcnt vmcnt(0)" ::: "memory");
;         } else {
;             XB_SPIN(xb_ld(&bar[XB_XGEN(b.x)]) == gen, bar);
.LBB0_181:
	s_or_b64 exec, exec, s[16:17]
	v_cvt_f32_u32_e32 v4, v2
	s_waitcnt vmcnt(0)
	v_readfirstlane_b32 s3, v3
	v_sub_u32_e32 v3, 0, v2
	v_rcp_iflag_f32_e32 v4, v4
	v_add_u32_e32 v5, s3, v1
	v_mul_f32_e32 v4, 0x4f7ffffe, v4
	v_cvt_u32_f32_e32 v4, v4
	v_mul_lo_u32 v1, v3, v4
	v_mul_hi_u32 v1, v4, v1
	v_add_u32_e32 v1, v4, v1
	v_mul_hi_u32 v1, v5, v1
	v_mul_lo_u32 v3, v1, v2
	v_sub_u32_e32 v3, v5, v3
	v_add_u32_e32 v4, 1, v1
	v_cmp_ge_u32_e32 vcc, v3, v2
	s_nop 1
	v_cndmask_b32_e32 v1, v1, v4, vcc
	v_sub_u32_e32 v4, v3, v2
	v_cndmask_b32_e32 v3, v3, v4, vcc
	v_add_u32_e32 v4, 1, v1
	v_cmp_ge_u32_e32 vcc, v3, v2
	v_add_u32_e32 v3, 1, v5
	s_nop 0
	v_cndmask_b32_e32 v1, v1, v4, vcc
	v_mul_lo_u32 v4, v2, v1
	v_add_u32_e32 v2, v4, v2
	v_cmp_ne_u32_e32 vcc, v3, v2
	s_and_saveexec_b64 s[4:5], vcc
	s_xor_b64 s[14:15], exec, s[4:5]
	s_cbranch_execz .LBB0_195
	s_waitcnt lgkmcnt(0)
	v_mov_b32_e32 v0, 0x3500
	global_load_dword v0, v0, s[34:35] sc1
	s_add_u32 s18, s34, 0x3500
	s_addc_u32 s19, s35, 0
	s_waitcnt vmcnt(0)
	v_cmp_eq_u32_e32 vcc, v0, v1
	s_and_saveexec_b64 s[16:17], vcc
	s_cbranch_execz .LBB0_194
	s_mov_b32 s3, 1
	s_mov_b64 s[20:21], 0
	v_mov_b32_e32 v0, 0
	s_branch .LBB0_185

; DI unsigned xb_add(unsigned* p, unsigned v) { return __hip_atomic_fetch_add(p, v, __ATOMIC_RELAXED, __HIP_MEMORY_SCOPE_AGENT); }
; DI void xcd_barrier(const XcdBarrier& b) {
;     ...
;             __builtin_amdgcn_fence(__ATOMIC_ACQUIRE, "agent");
;             xb_add(&bar[XB_XGEN(b.x)], 1u);
;             asm volatile("s_waitcnt vmcnt(0)" ::: "memory");
.LBB0_212:
	s_or_b64 exec, exec, s[14:15]
	s_mov_b64 s[14:15], exec
	v_mbcnt_lo_u32_b32 v0, s14, 0
	v_mbcnt_hi_u32_b32 v0, s15, v0
	v_cmp_eq_u32_e32 vcc, 0, v0
	s_waitcnt vmcnt(0)
	buffer_inv sc1
	s_and_saveexec_b64 s[16:17], vcc
	s_cbranch_execz .LBB0_214
	s_bcnt1_i32_b64 s3, s[14:15]
	v_mov_b32_e32 v0, 0x2000
	v_mov_b32_e32 v1, s3
.LBB0_214:
	s_or_b64 exec, exec, s[16:17]
	s_waitcnt vmcnt(0)

; DI unsigned xb_add(unsigned* p, unsigned v) { return __hip_atomic_fetch_add(p, v, __ATOMIC_RELAXED, __HIP_MEMORY_SCOPE_AGENT); }
; DI void xcd_barrier(const XcdBarrier& b) {
;     ...
;             __builtin_amdgcn_fence(__ATOMIC_ACQUIRE, "agent");
;             xb_add(&bar[XB_XGEN(b.x)], 1u);
;             asm volatile("s_waitcnt vmcnt(0)" ::: "memory");
.LBB0_267:
	s_or_b64 exec, exec, s[14:15]
	s_mov_b64 s[14:15], exec
	v_mbcnt_lo_u32_b32 v0, s14, 0
	v_mbcnt_hi_u32_b32 v0, s15, v0
	v_cmp_eq_u32_e32 vcc, 0, v0
	s_waitcnt vmcnt(0)
	buffer_inv sc1
	s_and_saveexec_b64 s[16:17], vcc
	s_cbranch_execz .LBB0_269
	s_bcnt1_i32_b64 s3, s[14:15]
	v_mov_b32_e32 v0, 0x2000
	v_mov_b32_e32 v1, s3
.LBB0_269:
	s_or_b64 exec, exec, s[16:17]
	s_waitcnt vmcnt(0)

; DI unsigned xb_add(unsigned* p, unsigned v) { return __hip_atomic_fetch_add(p, v, __ATOMIC_RELAXED, __HIP_MEMORY_SCOPE_AGENT); }
; DI void xcd_barrier(const XcdBarrier& b) {
;     ...
;             __builtin_amdgcn_fence(__ATOMIC_ACQUIRE, "agent");
;             xb_add(&bar[XB_XGEN(b.x)], 1u);
;             asm volatile("s_waitcnt vmcnt(0)" ::: "memory");
.LBB0_370:
	s_or_b64 exec, exec, s[10:11]
	s_mov_b64 s[10:11], exec
	v_mbcnt_lo_u32_b32 v0, s10, 0
	v_mbcnt_hi_u32_b32 v0, s11, v0
	v_cmp_eq_u32_e32 vcc, 0, v0
	s_waitcnt vmcnt(0)
	buffer_inv sc1
	s_and_saveexec_b64 s[12:13], vcc
	s_cbranch_execz .LBB0_372
	s_bcnt1_i32_b64 s3, s[10:11]
	v_mov_b32_e32 v0, 0x2000
	v_mov_b32_e32 v1, s3
.LBB0_372:
	s_or_b64 exec, exec, s[12:13]
	s_waitcnt vmcnt(0)

; DI unsigned xb_add(unsigned* p, unsigned v) { return __hip_atomic_fetch_add(p, v, __ATOMIC_RELAXED, __HIP_MEMORY_SCOPE_AGENT); }
; DI void xcd_barrier(const XcdBarrier& b) {
;     ...
;             __builtin_amdgcn_fence(__ATOMIC_ACQUIRE, "agent");
;             xb_add(&bar[XB_XGEN(b.x)], 1u);
;             asm volatile("s_waitcnt vmcnt(0)" ::: "memory");
.LBB0_432:
	s_or_b64 exec, exec, s[10:11]
	s_mov_b64 s[10:11], exec
	v_mbcnt_lo_u32_b32 v0, s10, 0
	v_mbcnt_hi_u32_b32 v0, s11, v0
	v_cmp_eq_u32_e32 vcc, 0, v0
	s_waitcnt vmcnt(0)
	buffer_inv sc1
	s_and_saveexec_b64 s[12:13], vcc
	s_cbranch_execz .LBB0_434
	s_bcnt1_i32_b64 s3, s[10:11]
	v_mov_b32_e32 v0, 0x2000
	v_mov_b32_e32 v1, s3
.LBB0_434:
	s_or_b64 exec, exec, s[12:13]
	s_waitcnt vmcnt(0)

; DI unsigned xb_ld(unsigned* p)              { return __hip_atomic_load(p, __ATOMIC_RELAXED, __HIP_MEMORY_SCOPE_AGENT); }
; DI unsigned xb_add(unsigned* p, unsigned v) { return __hip_atomic_fetch_add(p, v, __ATOMIC_RELAXED, __HIP_MEMORY_SCOPE_AGENT); }
; #define XB_SPIN(cond, bar) do { unsigned _sp = 0; while (cond) { __builtin_amdgcn_s_sleep(1); \
;     if ((++_sp & 255u) == 0u) { if (xb_ld(&(bar)[XB_TMO])) break; if (_sp > XB_SPIN_CAP) { atomicAdd(&(bar)[XB_TMO], 1u); break; } } } } while (0)
; DI void xcd_barrier(const XcdBarrier& b) {
;     ...
;         const unsigned old = xb_add(&bar[XB_XSUB(b.x)], 1u);
;         const unsigned gen = old / nloc;
;         if (old + 1u == (gen + 1u) * nloc) {
;             __builtin_amdgcn_fence(__ATOMIC_RELEASE, "agent");
;             asm volatile("s_waitcnt vmcnt(0)" ::: "memory");
;             const unsigned og = xb_add(&bar[XB_TOP], 1u);
;             const unsigned tg = og / nx;
;             if (og + 1u == (tg + 1u) * nx) xb_add(&bar[XB_TOPGEN], 1u);
;             else XB_SPIN(xb_ld(&bar[XB_TOPGEN]) == tg, bar);
;             __builtin_amdgcn_fence(__ATOMIC_ACQUIRE, "agent");
;             xb_add(&bar[XB_XGEN(b.x)], 1u);
;             asm volatile("s_waitcnt vmcnt(0)" ::: "memory");
;         } else {
;             XB_SPIN(xb_ld(&bar[XB_XGEN(b.x)]) == gen, bar);
.LBB0_474:
	s_or_b64 exec, exec, s[14:15]
	v_cvt_f32_u32_e32 v4, v2
	s_waitcnt vmcnt(0)
	v_readfirstlane_b32 s4, v3
	v_sub_u32_e32 v3, 0, v2
	v_rcp_iflag_f32_e32 v4, v4
	v_add_u32_e32 v5, s4, v1
	v_mul_f32_e32 v4, 0x4f7ffffe, v4
	v_cvt_u32_f32_e32 v4, v4
	v_mul_lo_u32 v1, v3, v4
	v_mul_hi_u32 v1, v4, v1
	v_add_u32_e32 v1, v4, v1
	v_mul_hi_u32 v1, v5, v1
	v_mul_lo_u32 v3, v1, v2
	v_sub_u32_e32 v3, v5, v3
	v_add_u32_e32 v4, 1, v1
	v_cmp_ge_u32_e32 vcc, v3, v2
	s_nop 1
	v_cndmask_b32_e32 v1, v1, v4, vcc
	v_sub_u32_e32 v4, v3, v2
	v_cndmask_b32_e32 v3, v3, v4, vcc
	v_add_u32_e32 v4, 1, v1
	v_cmp_ge_u32_e32 vcc, v3, v2
	v_add_u32_e32 v3, 1, v5
	s_nop 0
	v_cndmask_b32_e32 v1, v1, v4, vcc
	v_mul_lo_u32 v4, v2, v1
	v_add_u32_e32 v2, v4, v2
	v_cmp_ne_u32_e32 vcc, v3, v2
	s_and_saveexec_b64 s[4:5], vcc
	s_xor_b64 s[12:13], exec, s[4:5]
	s_cbranch_execz .LBB0_488
	s_waitcnt lgkmcnt(0)
	v_mov_b32_e32 v0, 0x3500
	global_load_dword v0, v0, s[34:35] sc1
	s_add_u32 s16, s34, 0x3500
	s_addc_u32 s17, s35, 0
	s_waitcnt vmcnt(0)
	v_cmp_eq_u32_e32 vcc, v0, v1
	s_and_saveexec_b64 s[14:15], vcc
	s_cbranch_execz .LBB0_487
	s_mov_b32 s4, 1
	s_mov_b64 s[18:19], 0
	v_mov_b32_e32 v0, 0
	s_branch .LBB0_478

; DI unsigned xb_add(unsigned* p, unsigned v) { return __hip_atomic_fetch_add(p, v, __ATOMIC_RELAXED, __HIP_MEMORY_SCOPE_AGENT); }
; DI void xcd_barrier(const XcdBarrier& b) {
;     ...
;             __builtin_amdgcn_fence(__ATOMIC_ACQUIRE, "agent");
;             xb_add(&bar[XB_XGEN(b.x)], 1u);
;             asm volatile("s_waitcnt vmcnt(0)" ::: "memory");
.LBB0_505:
	s_or_b64 exec, exec, s[12:13]
	s_mov_b64 s[12:13], exec
	v_mbcnt_lo_u32_b32 v0, s12, 0
	v_mbcnt_hi_u32_b32 v0, s13, v0
	v_cmp_eq_u32_e32 vcc, 0, v0
	s_waitcnt vmcnt(0)
	buffer_inv sc1
	s_and_saveexec_b64 s[14:15], vcc
	s_cbranch_execz .LBB0_507
	s_bcnt1_i32_b64 s4, s[12:13]
	v_mov_b32_e32 v0, 0x2000
	v_mov_b32_e32 v1, s4
.LBB0_507:
	s_or_b64 exec, exec, s[14:15]
	s_waitcnt vmcnt(0)

; DI unsigned xb_add(unsigned* p, unsigned v) { return __hip_atomic_fetch_add(p, v, __ATOMIC_RELAXED, __HIP_MEMORY_SCOPE_AGENT); }
; DI void xcd_barrier(const XcdBarrier& b) {
;     ...
;             __builtin_amdgcn_fence(__ATOMIC_ACQUIRE, "agent");
;             xb_add(&bar[XB_XGEN(b.x)], 1u);
;             asm volatile("s_waitcnt vmcnt(0)" ::: "memory");
.LBB0_713:
	s_or_b64 exec, exec, s[12:13]
	s_mov_b64 s[12:13], exec
	v_mbcnt_lo_u32_b32 v0, s12, 0
	v_mbcnt_hi_u32_b32 v0, s13, v0
	v_cmp_eq_u32_e32 vcc, 0, v0
	s_waitcnt vmcnt(0)
	buffer_inv sc1
	s_and_saveexec_b64 s[14:15], vcc
	s_cbranch_execz .LBB0_715
	s_bcnt1_i32_b64 s4, s[12:13]
	v_mov_b32_e32 v0, 0x2000
	v_mov_b32_e32 v1, s4
.LBB0_715:
	s_or_b64 exec, exec, s[14:15]
	s_waitcnt vmcnt(0)

; DI unsigned xb_ld(unsigned* p)              { return __hip_atomic_load(p, __ATOMIC_RELAXED, __HIP_MEMORY_SCOPE_AGENT); }
; DI unsigned xb_add(unsigned* p, unsigned v) { return __hip_atomic_fetch_add(p, v, __ATOMIC_RELAXED, __HIP_MEMORY_SCOPE_AGENT); }
; #define XB_SPIN(cond, bar) do { unsigned _sp = 0; while (cond) { __builtin_amdgcn_s_sleep(1); \
;     if ((++_sp & 255u) == 0u) { if (xb_ld(&(bar)[XB_TMO])) break; if (_sp > XB_SPIN_CAP) { atomicAdd(&(bar)[XB_TMO], 1u); break; } } } } while (0)
; DI void xcd_barrier(const XcdBarrier& b) {
;     ...
;         const unsigned old = xb_add(&bar[XB_XSUB(b.x)], 1u);
;         const unsigned gen = old / nloc;
;         if (old + 1u == (gen + 1u) * nloc) {
;             __builtin_amdgcn_fence(__ATOMIC_RELEASE, "agent");
;             asm volatile("s_waitcnt vmcnt(0)" ::: "memory");
;             const unsigned og = xb_add(&bar[XB_TOP], 1u);
;             const unsigned tg = og / nx;
;             if (og + 1u == (tg + 1u) * nx) xb_add(&bar[XB_TOPGEN], 1u);
;             else XB_SPIN(xb_ld(&bar[XB_TOPGEN]) == tg, bar);
;             __builtin_amdgcn_fence(__ATOMIC_ACQUIRE, "agent");
;             xb_add(&bar[XB_XGEN(b.x)], 1u);
;             asm volatile("s_waitcnt vmcnt(0)" ::: "memory");
;         } else {
;             XB_SPIN(xb_ld(&bar[XB_XGEN(b.x)]) == gen, bar);
.LBB0_938:
	s_or_b64 exec, exec, s[16:17]
	v_cvt_f32_u32_e32 v4, v2
	s_waitcnt vmcnt(0)
	v_readfirstlane_b32 s4, v3
	v_sub_u32_e32 v3, 0, v2
	v_rcp_iflag_f32_e32 v4, v4
	v_add_u32_e32 v5, s4, v1
	v_mul_f32_e32 v4, 0x4f7ffffe, v4
	v_cvt_u32_f32_e32 v4, v4
	v_mul_lo_u32 v1, v3, v4
	v_mul_hi_u32 v1, v4, v1
	v_add_u32_e32 v1, v4, v1
	v_mul_hi_u32 v1, v5, v1
	v_mul_lo_u32 v3, v1, v2
	v_sub_u32_e32 v3, v5, v3
	v_add_u32_e32 v4, 1, v1
	v_cmp_ge_u32_e32 vcc, v3, v2
	s_nop 1
	v_cndmask_b32_e32 v1, v1, v4, vcc
	v_sub_u32_e32 v4, v3, v2
	v_cndmask_b32_e32 v3, v3, v4, vcc
	v_add_u32_e32 v4, 1, v1
	v_cmp_ge_u32_e32 vcc, v3, v2
	v_add_u32_e32 v3, 1, v5
	s_nop 0
	v_cndmask_b32_e32 v1, v1, v4, vcc
	v_mul_lo_u32 v4, v2, v1
	v_add_u32_e32 v2, v4, v2
	v_cmp_ne_u32_e32 vcc, v3, v2
	s_and_saveexec_b64 s[4:5], vcc
	s_xor_b64 s[14:15], exec, s[4:5]
	s_cbranch_execz .LBB0_952
	s_waitcnt lgkmcnt(0)
	v_mov_b32_e32 v0, 0x3500
	global_load_dword v0, v0, s[34:35] sc1
	s_add_u32 s18, s34, 0x3500
	s_addc_u32 s19, s35, 0
	s_waitcnt vmcnt(0)
	v_cmp_eq_u32_e32 vcc, v0, v1
	s_and_saveexec_b64 s[16:17], vcc
	s_cbranch_execz .LBB0_951
	s_mov_b32 s4, 1
	s_mov_b64 s[20:21], 0
	v_mov_b32_e32 v0, 0
	s_branch .LBB0_942

; DI unsigned xb_add(unsigned* p, unsigned v) { return __hip_atomic_fetch_add(p, v, __ATOMIC_RELAXED, __HIP_MEMORY_SCOPE_AGENT); }
; DI void xcd_barrier(const XcdBarrier& b) {
;     ...
;             __builtin_amdgcn_fence(__ATOMIC_ACQUIRE, "agent");
;             xb_add(&bar[XB_XGEN(b.x)], 1u);
;             asm volatile("s_waitcnt vmcnt(0)" ::: "memory");
.LBB0_969:
	s_or_b64 exec, exec, s[14:15]
	s_mov_b64 s[14:15], exec
	v_mbcnt_lo_u32_b32 v0, s14, 0
	v_mbcnt_hi_u32_b32 v0, s15, v0
	v_cmp_eq_u32_e32 vcc, 0, v0
	s_waitcnt vmcnt(0)
	buffer_inv sc1
	s_and_saveexec_b64 s[16:17], vcc
	s_cbranch_execz .LBB0_971
	s_bcnt1_i32_b64 s4, s[14:15]
	v_mov_b32_e32 v0, 0x2000
	v_mov_b32_e32 v1, s4
.LBB0_971:
	s_or_b64 exec, exec, s[16:17]
	s_waitcnt vmcnt(0)

; DI unsigned xb_ld(unsigned* p)              { return __hip_atomic_load(p, __ATOMIC_RELAXED, __HIP_MEMORY_SCOPE_AGENT); }
; DI unsigned xb_add(unsigned* p, unsigned v) { return __hip_atomic_fetch_add(p, v, __ATOMIC_RELAXED, __HIP_MEMORY_SCOPE_AGENT); }
; #define XB_SPIN(cond, bar) do { unsigned _sp = 0; while (cond) { __builtin_amdgcn_s_sleep(1); \
;     if ((++_sp & 255u) == 0u) { if (xb_ld(&(bar)[XB_TMO])) break; if (_sp > XB_SPIN_CAP) { atomicAdd(&(bar)[XB_TMO], 1u); break; } } } } while (0)
; DI void xcd_barrier(const XcdBarrier& b) {
;     ...
;         const unsigned old = xb_add(&bar[XB_XSUB(b.x)], 1u);
;         const unsigned gen = old / nloc;
;         if (old + 1u == (gen + 1u) * nloc) {
;             __builtin_amdgcn_fence(__ATOMIC_RELEASE, "agent");
;             asm volatile("s_waitcnt vmcnt(0)" ::: "memory");
;             const unsigned og = xb_add(&bar[XB_TOP], 1u);
;             const unsigned tg = og / nx;
;             if (og + 1u == (tg + 1u) * nx) xb_add(&bar[XB_TOPGEN], 1u);
;             else XB_SPIN(xb_ld(&bar[XB_TOPGEN]) == tg, bar);
;             __builtin_amdgcn_fence(__ATOMIC_ACQUIRE, "agent");
;             xb_add(&bar[XB_XGEN(b.x)], 1u);
;             asm volatile("s_waitcnt vmcnt(0)" ::: "memory");
;         } else {
;             XB_SPIN(xb_ld(&bar[XB_XGEN(b.x)]) == gen, bar);
.LBB0_999:
	s_or_b64 exec, exec, s[12:13]
	v_cvt_f32_u32_e32 v4, v2
	s_waitcnt vmcnt(0)
	v_readfirstlane_b32 s2, v3
	v_sub_u32_e32 v3, 0, v2
	v_rcp_iflag_f32_e32 v4, v4
	v_add_u32_e32 v5, s2, v1
	v_mul_f32_e32 v4, 0x4f7ffffe, v4
	v_cvt_u32_f32_e32 v4, v4
	v_mul_lo_u32 v1, v3, v4
	v_mul_hi_u32 v1, v4, v1
	v_add_u32_e32 v1, v4, v1
	v_mul_hi_u32 v1, v5, v1
	v_mul_lo_u32 v3, v1, v2
	v_sub_u32_e32 v3, v5, v3
	v_add_u32_e32 v4, 1, v1
	v_cmp_ge_u32_e32 vcc, v3, v2
	s_nop 1
	v_cndmask_b32_e32 v1, v1, v4, vcc
	v_sub_u32_e32 v4, v3, v2
	v_cndmask_b32_e32 v3, v3, v4, vcc
	v_add_u32_e32 v4, 1, v1
	v_cmp_ge_u32_e32 vcc, v3, v2
	v_add_u32_e32 v3, 1, v5
	s_nop 0
	v_cndmask_b32_e32 v1, v1, v4, vcc
	v_mul_lo_u32 v4, v2, v1
	v_add_u32_e32 v2, v4, v2
	v_cmp_ne_u32_e32 vcc, v3, v2
	s_and_saveexec_b64 s[2:3], vcc
	s_xor_b64 s[10:11], exec, s[2:3]
	s_cbranch_execz .LBB0_1013
	s_waitcnt lgkmcnt(0)
	v_mov_b32_e32 v0, 0x3500
	global_load_dword v0, v0, s[34:35] sc1
	s_add_u32 s14, s34, 0x3500
	s_addc_u32 s15, s35, 0
	s_waitcnt vmcnt(0)
	v_cmp_eq_u32_e32 vcc, v0, v1
	s_and_saveexec_b64 s[12:13], vcc
	s_cbranch_execz .LBB0_1012
	s_mov_b32 s2, 1
	s_mov_b64 s[16:17], 0
	v_mov_b32_e32 v0, 0
	s_branch .LBB0_1003

; DI unsigned xb_add(unsigned* p, unsigned v) { return __hip_atomic_fetch_add(p, v, __ATOMIC_RELAXED, __HIP_MEMORY_SCOPE_AGENT); }
; DI void xcd_barrier(const XcdBarrier& b) {
;     ...
;             __builtin_amdgcn_fence(__ATOMIC_ACQUIRE, "agent");
;             xb_add(&bar[XB_XGEN(b.x)], 1u);
;             asm volatile("s_waitcnt vmcnt(0)" ::: "memory");
.LBB0_1030:
	s_or_b64 exec, exec, s[10:11]
	s_mov_b64 s[10:11], exec
	v_mbcnt_lo_u32_b32 v0, s10, 0
	v_mbcnt_hi_u32_b32 v0, s11, v0
	v_cmp_eq_u32_e32 vcc, 0, v0
	s_waitcnt vmcnt(0)
	buffer_inv sc1
	s_and_saveexec_b64 s[12:13], vcc
	s_cbranch_execz .LBB0_1032
	s_bcnt1_i32_b64 s2, s[10:11]
	v_mov_b32_e32 v0, 0x2000
	v_mov_b32_e32 v1, s2
.LBB0_1032:
	s_or_b64 exec, exec, s[12:13]
	s_waitcnt vmcnt(0)
